# norm2 sweep: vmcnt(0) moved into rare batch-boundary load path
# baseline (speedup 1.0000x reference)
.LBB0_1391:
	v_cvt_f32_fp8_e32 v118, v116
	v_cvt_f32_fp8_sdwa v119, v116 src0_sel:BYTE_1
	v_cvt_f32_fp8_sdwa v148, v116 src0_sel:BYTE_2
	v_cvt_f32_fp8_sdwa v149, v116 src0_sel:BYTE_3
	v_sub_f32_e32 v112, v112, v118
	v_sub_f32_e32 v113, v113, v119
	v_cvt_pk_bf16_f32 v112, v112, v113
	v_sub_f32_e32 v113, v114, v148
	v_cvt_pk_bf16_f32 v116, v118, v119
	v_cvt_pk_bf16_f32 v117, v148, v149
	ds_write_b64 v182, v[116:117] offset:1536
	v_sub_f32_e32 v114, v115, v149
	v_cvt_pk_bf16_f32 v113, v113, v114
	ds_write_b64 v183, v[112:113] offset:1536
	s_waitcnt lgkmcnt(0)
	s_barrier
	ds_read_b128 v[112:115], v172
	ds_read_b128 v[148:151], v172 offset:64
	s_waitcnt lgkmcnt(1)
	v_mfma_f32_16x16x32_bf16 v[116:119], v[56:59], v[112:115], 0
	ds_read_b128 v[152:155], v172 offset:128
	ds_read_b128 v[156:159], v172 offset:192
	ds_read_b128 v[160:163], v172 offset:320
	s_waitcnt lgkmcnt(3)
	v_mfma_f32_16x16x32_bf16 v[116:119], v[60:63], v[148:151], v[116:119]
	ds_read_b128 v[164:167], v172 offset:384
	ds_read_b128 v[168:171], v172 offset:448
	ds_read_b128 v[174:177], v185
	v_mfma_f32_16x16x32_bf16 v[112:115], v[48:51], v[112:115], 0
	s_add_i32 s19, s19, -1
	s_cmp_eq_u32 s19, 0
	s_mov_b32 s21, s20
	s_waitcnt lgkmcnt(5)
	v_mfma_f32_16x16x32_bf16 v[116:119], v[72:75], v[152:155], v[116:119]
	v_mfma_f32_16x16x32_bf16 v[112:115], v[52:55], v[148:151], v[112:115]
	ds_read_b128 v[148:151], v172 offset:256
	s_waitcnt lgkmcnt(5)
	v_mfma_f32_16x16x32_bf16 v[116:119], v[76:79], v[156:159], v[116:119]
	s_waitcnt lgkmcnt(0)
	v_mfma_f32_16x16x32_bf16 v[116:119], v[88:91], v[148:151], v[116:119]
	v_mfma_f32_16x16x32_bf16 v[116:119], v[92:95], v[160:163], v[116:119]
	v_mfma_f32_16x16x32_bf16 v[116:119], v[104:107], v[164:167], v[116:119]
	v_mfma_f32_16x16x32_bf16 v[116:119], v[108:111], v[168:171], v[116:119]
	v_mfma_f32_16x16x32_bf16 v[116:119], v[48:51], v[174:177], v[116:119]
	ds_read_b128 v[174:177], v185 offset:64
	s_waitcnt lgkmcnt(0)
	v_mfma_f32_16x16x32_bf16 v[116:119], v[52:55], v[174:177], v[116:119]
	ds_read_b128 v[174:177], v185 offset:128
	s_waitcnt lgkmcnt(0)
	v_mfma_f32_16x16x32_bf16 v[116:119], v[64:67], v[174:177], v[116:119]
	ds_read_b128 v[174:177], v185 offset:192
	s_waitcnt lgkmcnt(0)
	v_mfma_f32_16x16x32_bf16 v[116:119], v[68:71], v[174:177], v[116:119]
	ds_read_b128 v[174:177], v185 offset:256
	v_mfma_f32_16x16x32_bf16 v[112:115], v[64:67], v[152:155], v[112:115]
	s_waitcnt vmcnt(0)
	v_mov_b64_e32 v[152:153], v[140:141]
	v_mov_b64_e32 v[154:155], v[146:147]
	v_mfma_f32_16x16x32_bf16 v[112:115], v[68:71], v[156:159], v[112:115]
	s_waitcnt lgkmcnt(0)
	v_mfma_f32_16x16x32_bf16 v[116:119], v[80:83], v[174:177], v[116:119]
	ds_read_b128 v[174:177], v185 offset:320
	v_mfma_f32_16x16x32_bf16 v[112:115], v[80:83], v[148:151], v[112:115]
	v_mov_b64_e32 v[150:151], v[142:143]
	v_mov_b64_e32 v[148:149], v[144:145]
	s_waitcnt lgkmcnt(0)
	v_mfma_f32_16x16x32_bf16 v[116:119], v[84:87], v[174:177], v[116:119]
	ds_read_b128 v[174:177], v185 offset:384
	v_mfma_f32_16x16x32_bf16 v[112:115], v[84:87], v[160:163], v[112:115]
	s_waitcnt lgkmcnt(0)
	v_mfma_f32_16x16x32_bf16 v[116:119], v[96:99], v[174:177], v[116:119]
	ds_read_b128 v[174:177], v185 offset:448
	v_mfma_f32_16x16x32_bf16 v[112:115], v[96:99], v[164:167], v[112:115]
	s_waitcnt lgkmcnt(0)
	v_mfma_f32_16x16x32_bf16 v[116:119], v[100:103], v[174:177], v[116:119]
	v_mfma_f32_16x16x32_bf16 v[112:115], v[100:103], v[168:171], v[112:115]
	s_nop 7
	v_pk_add_f32 v[112:113], v[116:117], v[112:113]
	v_pk_add_f32 v[114:115], v[118:119], v[114:115]
	ds_write2_b32 v184, v112, v113 offset1:1
	ds_write2_b32 v184, v114, v115 offset0:2 offset1:3
	s_waitcnt lgkmcnt(0)
	s_barrier
	v_add_u32_e32 v184, 0x840, v184
	s_cbranch_scc1 .LBB0_1440
.LBB0_1392:
	s_waitcnt vmcnt(3)
	v_mov_b64_e32 v[112:113], v[134:135]
	s_waitcnt vmcnt(2)
	v_mov_b64_e32 v[114:115], v[132:133]
	s_waitcnt vmcnt(1)
	v_mov_b64_e32 v[116:117], v[130:131]
	s_waitcnt vmcnt(0)
	v_mov_b64_e32 v[118:119], v[128:129]
	s_add_i32 s20, s21, 16
	s_min_i32 s2, s20, s18
	s_ashr_i32 s3, s2, 31
	s_lshl_b64 s[2:3], s[2:3], 11
	v_lshl_add_u64 v[134:135], v[124:125], 0, s[2:3]
	s_add_i32 s2, s21, 24
	s_min_i32 s2, s2, s18
	s_ashr_i32 s3, s2, 31
	s_lshl_b64 s[2:3], s[2:3], 11
	v_lshl_add_u64 v[146:147], v[124:125], 0, s[2:3]
	global_load_dwordx2 v[128:129], v[134:135], off
	global_load_dwordx2 v[130:131], v[134:135], off offset:512
	global_load_dwordx2 v[132:133], v[134:135], off offset:1024
	s_nop 0
	global_load_dwordx2 v[134:135], v[134:135], off offset:1536
	s_nop 0
	global_load_dwordx2 v[140:141], v[146:147], off
	global_load_dwordx2 v[142:143], v[146:147], off offset:512
	global_load_dwordx2 v[144:145], v[146:147], off offset:1024
	s_nop 0
	global_load_dwordx2 v[146:147], v[146:147], off offset:1536
	v_and_b32_e32 v177, 0xffff0000, v118
	v_and_b32_e32 v179, 0xffff0000, v119
	v_lshlrev_b32_e32 v159, 16, v112
	v_and_b32_e32 v157, 0xffff0000, v112
	v_lshlrev_b32_e32 v176, 16, v118
	v_lshlrev_b32_e32 v178, 16, v119
	v_mul_f32_e32 v112, v179, v179
	v_lshlrev_b32_e32 v162, 16, v114
	v_and_b32_e32 v163, 0xffff0000, v114
	v_mul_f32_e32 v114, v177, v177
	v_lshlrev_b32_e32 v160, 16, v113
	v_and_b32_e32 v161, 0xffff0000, v113
	v_pk_fma_f32 v[112:113], v[178:179], v[178:179], v[112:113] op_sel_hi:[1,1,0]
	v_and_b32_e32 v171, 0xffff0000, v117
	v_and_b32_e32 v170, 0xffff0000, v116
	v_lshlrev_b32_e32 v164, 16, v115
	v_and_b32_e32 v165, 0xffff0000, v115
	v_pk_fma_f32 v[114:115], v[176:177], v[176:177], v[114:115] op_sel_hi:[1,1,0]
	v_lshlrev_b32_e32 v169, 16, v117
	v_lshlrev_b32_e32 v168, 16, v116
	v_pk_mul_f32 v[116:117], v[170:171], v[170:171]
	v_mov_b32_e32 v158, v114
	v_mov_b32_e32 v118, v112
	v_mov_b32_e32 v119, v159
	v_pk_fma_f32 v[116:117], v[168:169], v[168:169], v[116:117]
	v_pk_add_f32 v[112:113], v[114:115], v[112:113]
	v_pk_mul_f32 v[114:115], v[158:159], v[118:119]
	v_mul_f32_e32 v156, v157, v157
	v_mov_b32_e32 v113, v115
	v_pk_add_f32 v[114:115], v[116:117], v[116:117] op_sel:[0,1] op_sel_hi:[1,0]
	v_mul_f32_e32 v116, v165, v165
	v_mov_b32_e32 v115, v156
	v_pk_add_f32 v[112:113], v[112:113], v[114:115]
	v_mul_f32_e32 v114, v163, v163
	v_mul_f32_e32 v166, v160, v160
	v_mul_f32_e32 v167, v161, v161
	v_pk_fma_f32 v[114:115], v[162:163], v[162:163], v[114:115] op_sel_hi:[1,1,0]
	v_pk_fma_f32 v[116:117], v[164:165], v[164:165], v[116:117] op_sel_hi:[1,1,0]
	s_min_i32 s6, s21, s18
	v_mov_b32_e32 v115, v166
	v_mov_b32_e32 v117, v167
	s_add_i32 s2, s6, 0xfffff800
	v_pk_add_f32 v[114:115], v[114:115], v[116:117]
	s_lshr_b32 s2, s2, 11
	v_pk_add_f32 v[112:113], v[112:113], v[114:115]
	s_cmpk_gt_i32 s6, 0x7ff
	v_add_f32_e32 v112, v112, v113
	s_cselect_b32 s7, s2, 8
	s_cmp_lg_u32 s7, s15
	v_add_f32_dpp v112, v112, v112 quad_perm:[1,0,3,2] row_mask:0xf bank_mask:0xf bound_ctrl:1
	s_cselect_b64 s[2:3], -1, 0
	s_add_u32 s4, s17, s7
	v_add_f32_dpp v112, v112, v112 quad_perm:[2,3,0,1] row_mask:0xf bank_mask:0xf bound_ctrl:1
	s_addc_u32 s5, s16, 0
	v_mov_b32_e32 v113, v173
	v_add_f32_dpp v112, v112, v112 row_half_mirror row_mask:0xf bank_mask:0xf bound_ctrl:1
	s_mulk_i32 s5, 0x6000
	s_mul_hi_u32 s8, s4, 0x6000
	v_add_f32_dpp v112, v112, v112 row_mirror row_mask:0xf bank_mask:0xf bound_ctrl:1
	s_add_i32 s8, s8, s5
	s_mulk_i32 s4, 0x6000
	v_mov_b32_dpp v113, v112 row_bcast:15 row_mask:0xa bank_mask:0xf
	v_add_f32_e32 v112, v112, v113
	v_mov_b32_e32 v113, v173
	s_add_u32 s4, s84, s4
	s_addc_u32 s5, s86, s8
	v_mov_b32_dpp v113, v112 row_bcast:31 row_mask:0xc bank_mask:0xf
	v_add_f32_e32 v112, v112, v113
	s_add_u32 s8, s4, 0x4000
	v_readlane_b32 s22, v112, 63
	s_addc_u32 s9, s5, 0
	v_mov_b64_e32 v[114:115], v[18:19]
	s_cmp_eq_u32 s7, s15
	v_mov_b64_e32 v[112:113], v[16:17]
	s_cbranch_scc1 .LBB0_1394
	v_lshl_add_u64 v[112:113], v[122:123], 2, s[8:9]
	global_load_dwordx4 v[112:115], v[112:113], off
	s_waitcnt vmcnt(0)
.LBB0_1394:
	v_lshl_add_u64 v[116:117], v[122:123], 2, s[4:5]
	s_mov_b64 s[4:5], 0x3000
	v_lshl_add_u64 v[166:167], v[116:117], 0, s[4:5]
	v_cndmask_b32_e64 v116, 0, 1, s[2:3]
	v_cmp_ne_u32_e64 s[4:5], 1, v116
	v_mov_b64_e32 v[118:119], v[22:23]
	s_andn2_b64 vcc, exec, s[2:3]
	v_mov_b64_e32 v[116:117], v[20:21]
	s_cbranch_vccnz .LBB0_1396
	global_load_dwordx4 v[116:119], v[166:167], off
	s_waitcnt vmcnt(0)
.LBB0_1396:
	v_fma_f32 v156, s22, v212, v198
	s_mov_b32 s0, 0x800000
	v_cmp_gt_f32_e32 vcc, s0, v156
	v_mul_f32_e32 v158, 0x4b800000, v156
	v_pk_add_f32 v[114:115], v[114:115], 1.0 op_sel_hi:[1,0]
	v_cndmask_b32_e32 v156, v156, v158, vcc
	v_rsq_f32_e32 v156, v156
	v_pk_add_f32 v[186:187], v[112:113], 1.0 op_sel_hi:[1,0]
	s_cmp_lt_i32 s21, s1
	s_cselect_b64 s[10:11], -1, 0
	v_mul_f32_e32 v158, 0x45800000, v156
	v_cndmask_b32_e32 v174, v156, v158, vcc
	v_pk_mul_f32 v[178:179], v[174:175], v[178:179] op_sel_hi:[0,1]
	v_pk_mul_f32 v[176:177], v[174:175], v[176:177] op_sel_hi:[0,1]
	v_pk_mul_f32 v[176:177], v[0:1], v[176:177]
	v_pk_mul_f32 v[178:179], v[2:3], v[178:179]
	s_ashr_i32 s7, s6, 31
	v_pk_fma_f32 v[112:113], v[178:179], v[114:115], v[118:119]
	v_pk_fma_f32 v[114:115], v[176:177], v[186:187], v[116:117]
	v_mov_b32_e32 v116, v173
	v_cvt_pk_fp8_f32 v116, v114, v115
	s_lshl_b64 s[2:3], s[6:7], 10
	v_readlane_b32 s6, v253, 44
	v_readlane_b32 s7, v253, 45
	v_cvt_pk_fp8_f32 v116, v112, v113 op_sel:[0,0,1]
	s_add_u32 s6, s6, s2
	s_addc_u32 s7, s7, s3
	s_cmp_ge_i32 s21, s1
	v_lshl_add_u64 v[176:177], s[6:7], 0, v[122:123]
	s_cbranch_scc1 .LBB0_1398
	global_store_dword v[176:177], v116, off
.LBB0_1398:
	v_cvt_f32_fp8_e32 v118, v116
	v_cvt_f32_fp8_sdwa v119, v116 src0_sel:BYTE_1
	v_cvt_f32_fp8_sdwa v156, v116 src0_sel:BYTE_2
	v_cvt_f32_fp8_sdwa v158, v116 src0_sel:BYTE_3
	v_sub_f32_e32 v114, v114, v118
	v_sub_f32_e32 v115, v115, v119
	v_cvt_pk_bf16_f32 v114, v114, v115
	v_sub_f32_e32 v112, v112, v156
	v_sub_f32_e32 v113, v113, v158
	v_cvt_pk_bf16_f32 v115, v112, v113
	v_cvt_pk_bf16_f32 v116, v118, v119
	v_cvt_pk_bf16_f32 v117, v156, v158
	ds_write_b64 v180, v[116:117]
	ds_write_b64 v181, v[114:115]
	v_mov_b64_e32 v[114:115], v[26:27]
	s_and_b64 vcc, exec, s[4:5]
	v_mov_b64_e32 v[112:113], v[24:25]
	s_cbranch_vccnz .LBB0_1400
	v_lshl_add_u64 v[112:113], v[126:127], 2, s[8:9]
	global_load_dwordx4 v[112:115], v[112:113], off
	s_waitcnt vmcnt(0)
.LBB0_1400:
	v_mov_b64_e32 v[118:119], v[34:35]
	s_and_b64 vcc, exec, s[4:5]
	v_mov_b64_e32 v[116:117], v[32:33]
	s_cbranch_vccnz .LBB0_1402
	global_load_dwordx4 v[116:119], v[166:167], off offset:1024
	s_waitcnt vmcnt(0)
.LBB0_1402:
	v_mov_b32_e32 v175, v174
	v_mov_b32_e32 v178, v169
	v_mov_b32_e32 v169, v170
	v_pk_mul_f32 v[168:169], v[174:175], v[168:169]
	v_pk_add_f32 v[112:113], v[112:113], 1.0 op_sel_hi:[1,0]
	v_pk_mul_f32 v[168:169], v[4:5], v[168:169]
	v_mov_b32_e32 v179, v171
	v_pk_fma_f32 v[112:113], v[168:169], v[112:113], v[116:117]
	v_mov_b32_e32 v116, v173
	v_mov_b32_e32 v186, v174
	v_mov_b32_e32 v187, v174
	v_cvt_pk_fp8_f32 v116, v112, v113
	v_pk_mul_f32 v[178:179], v[186:187], v[178:179]
	v_pk_add_f32 v[114:115], v[114:115], 1.0 op_sel_hi:[1,0]
	v_pk_mul_f32 v[168:169], v[6:7], v[178:179]
	v_cndmask_b32_e64 v117, 0, 1, s[10:11]
	v_pk_fma_f32 v[114:115], v[168:169], v[114:115], v[118:119]
	v_cmp_ne_u32_e64 s[6:7], 1, v117
	v_cvt_pk_fp8_f32 v116, v114, v115 op_sel:[0,0,1]
	s_andn2_b64 vcc, exec, s[10:11]
	s_cbranch_vccnz .LBB0_1404
	global_store_dword v[176:177], v116, off offset:256
.LBB0_1404:
	v_cvt_f32_fp8_e32 v118, v116
	v_cvt_f32_fp8_sdwa v119, v116 src0_sel:BYTE_1
	v_cvt_f32_fp8_sdwa v156, v116 src0_sel:BYTE_2
	v_cvt_f32_fp8_sdwa v158, v116 src0_sel:BYTE_3
	v_sub_f32_e32 v112, v112, v118
	v_sub_f32_e32 v113, v113, v119
	v_cvt_pk_bf16_f32 v112, v112, v113
	v_sub_f32_e32 v113, v114, v156
	v_sub_f32_e32 v114, v115, v158
	v_cvt_pk_bf16_f32 v113, v113, v114
	v_cvt_pk_bf16_f32 v116, v118, v119
	v_cvt_pk_bf16_f32 v117, v156, v158
	ds_write_b64 v180, v[116:117] offset:512
	ds_write_b64 v181, v[112:113] offset:512
	v_mov_b64_e32 v[114:115], v[30:31]
	s_and_b64 vcc, exec, s[4:5]
	v_mov_b64_e32 v[112:113], v[28:29]
	s_cbranch_vccnz .LBB0_1406
	v_lshl_add_u64 v[112:113], v[136:137], 2, s[8:9]
	global_load_dwordx4 v[112:115], v[112:113], off
	s_waitcnt vmcnt(0)
.LBB0_1406:
	v_mov_b64_e32 v[118:119], v[42:43]
	s_and_b64 vcc, exec, s[4:5]
	v_mov_b64_e32 v[116:117], v[40:41]
	s_cbranch_vccnz .LBB0_1408
	global_load_dwordx4 v[116:119], v[166:167], off offset:2048
	s_waitcnt vmcnt(0)
.LBB0_1408:
	v_pk_mul_f32 v[162:163], v[174:175], v[162:163]
	v_pk_add_f32 v[112:113], v[112:113], 1.0 op_sel_hi:[1,0]
	v_pk_mul_f32 v[162:163], v[8:9], v[162:163]
	v_mov_b32_e32 v168, v174
	v_pk_fma_f32 v[112:113], v[162:163], v[112:113], v[116:117]
	v_mov_b32_e32 v116, v173
	v_mov_b32_e32 v169, v174
	v_cvt_pk_fp8_f32 v116, v112, v113
	v_pk_mul_f32 v[164:165], v[168:169], v[164:165]
	v_pk_add_f32 v[114:115], v[114:115], 1.0 op_sel_hi:[1,0]
	v_pk_mul_f32 v[162:163], v[10:11], v[164:165]
	s_and_b64 vcc, exec, s[6:7]
	v_pk_fma_f32 v[114:115], v[162:163], v[114:115], v[118:119]
	s_nop 0
	v_cvt_pk_fp8_f32 v116, v114, v115 op_sel:[0,0,1]
	s_cbranch_vccnz .LBB0_1410
	global_store_dword v[176:177], v116, off offset:512
.LBB0_1410:
	v_cvt_f32_fp8_e32 v118, v116
	v_cvt_f32_fp8_sdwa v119, v116 src0_sel:BYTE_1
	v_cvt_f32_fp8_sdwa v156, v116 src0_sel:BYTE_2
	v_cvt_f32_fp8_sdwa v158, v116 src0_sel:BYTE_3
	v_sub_f32_e32 v112, v112, v118
	v_sub_f32_e32 v113, v113, v119
	v_cvt_pk_bf16_f32 v112, v112, v113
	v_sub_f32_e32 v113, v114, v156
	v_sub_f32_e32 v114, v115, v158
	v_cvt_pk_bf16_f32 v113, v113, v114
	v_cvt_pk_bf16_f32 v116, v118, v119
	v_cvt_pk_bf16_f32 v117, v156, v158
	ds_write_b64 v180, v[116:117] offset:1024
	ds_write_b64 v181, v[112:113] offset:1024
	v_mov_b64_e32 v[114:115], v[38:39]
	s_and_b64 vcc, exec, s[4:5]
	v_mov_b64_e32 v[112:113], v[36:37]
	s_cbranch_vccnz .LBB0_1412
	v_lshl_add_u64 v[112:113], v[138:139], 2, s[8:9]
	global_load_dwordx4 v[112:115], v[112:113], off
	s_waitcnt vmcnt(0)
.LBB0_1412:
	v_mov_b64_e32 v[118:119], v[46:47]
	s_and_b64 vcc, exec, s[4:5]
	v_mov_b64_e32 v[116:117], v[44:45]
	s_cbranch_vccnz .LBB0_1414
	global_load_dwordx4 v[116:119], v[166:167], off offset:3072
	s_waitcnt vmcnt(0)
.LBB0_1414:
	v_mov_b32_e32 v156, v159
	v_pk_mul_f32 v[156:157], v[156:157], v[174:175]
	v_pk_add_f32 v[112:113], v[112:113], 1.0 op_sel_hi:[1,0]
	v_pk_mul_f32 v[156:157], v[12:13], v[156:157]
	v_mov_b32_e32 v162, v174
	v_pk_fma_f32 v[112:113], v[156:157], v[112:113], v[116:117]
	v_mov_b32_e32 v116, v173
	v_mov_b32_e32 v163, v174
	v_cvt_pk_fp8_f32 v116, v112, v113
	v_pk_mul_f32 v[160:161], v[160:161], v[162:163]
	v_pk_add_f32 v[114:115], v[114:115], 1.0 op_sel_hi:[1,0]
	v_pk_mul_f32 v[156:157], v[14:15], v[160:161]
	s_and_b64 vcc, exec, s[6:7]
	v_pk_fma_f32 v[114:115], v[156:157], v[114:115], v[118:119]
	s_nop 0
	v_cvt_pk_fp8_f32 v116, v114, v115 op_sel:[0,0,1]
	s_cbranch_vccnz .LBB0_1416
	global_store_dword v[176:177], v116, off offset:768
.LBB0_1416:
	v_cvt_f32_fp8_e32 v118, v116
	v_cvt_f32_fp8_sdwa v119, v116 src0_sel:BYTE_1
	v_cvt_f32_fp8_sdwa v156, v116 src0_sel:BYTE_2
	v_cvt_f32_fp8_sdwa v157, v116 src0_sel:BYTE_3
	v_sub_f32_e32 v112, v112, v118
	v_sub_f32_e32 v113, v113, v119
	v_cvt_pk_bf16_f32 v116, v118, v119
	v_cvt_pk_bf16_f32 v112, v112, v113
	v_sub_f32_e32 v113, v114, v156
	v_and_b32_e32 v167, 0xffff0000, v152
	v_and_b32_e32 v169, 0xffff0000, v153
	v_cvt_pk_bf16_f32 v117, v156, v157
	ds_write_b64 v180, v[116:117] offset:1536
	v_sub_f32_e32 v114, v115, v157
	v_cvt_pk_bf16_f32 v113, v113, v114
	ds_write_b64 v181, v[112:113] offset:1536
	v_lshlrev_b32_e32 v166, 16, v152
	v_lshlrev_b32_e32 v168, 16, v153
	v_mul_f32_e32 v112, v169, v169
	v_and_b32_e32 v163, 0xffff0000, v151
	v_and_b32_e32 v162, 0xffff0000, v150
	v_mul_f32_e32 v116, v167, v167
	v_lshlrev_b32_e32 v159, 16, v154
	v_pk_fma_f32 v[112:113], v[168:169], v[168:169], v[112:113] op_sel_hi:[1,1,0]
	v_lshlrev_b32_e32 v161, 16, v151
	v_lshlrev_b32_e32 v160, 16, v150
	v_pk_mul_f32 v[114:115], v[162:163], v[162:163]
	v_pk_fma_f32 v[116:117], v[166:167], v[166:167], v[116:117] op_sel_hi:[1,1,0]
	v_and_b32_e32 v157, 0xffff0000, v154
	v_pk_fma_f32 v[114:115], v[160:161], v[160:161], v[114:115]
	v_mov_b32_e32 v158, v116
	v_mov_b32_e32 v118, v112
	v_mov_b32_e32 v119, v159
	v_mul_f32_e32 v152, v157, v157
	v_pk_add_f32 v[112:113], v[116:117], v[112:113]
	v_pk_mul_f32 v[116:117], v[158:159], v[118:119]
	v_pk_add_f32 v[114:115], v[114:115], v[114:115] op_sel:[0,1] op_sel_hi:[1,0]
	v_lshlrev_b32_e32 v150, 16, v148
	v_and_b32_e32 v151, 0xffff0000, v148
	v_lshlrev_b32_e32 v148, 16, v149
	v_and_b32_e32 v149, 0xffff0000, v149
	v_mov_b32_e32 v113, v117
	v_mov_b32_e32 v115, v152
	s_add_i32 s21, s21, 8
	v_lshlrev_b32_e32 v154, 16, v155
	v_and_b32_e32 v155, 0xffff0000, v155
	v_pk_add_f32 v[112:113], v[112:113], v[114:115]
	v_mul_f32_e32 v114, v151, v151
	v_mul_f32_e32 v116, v149, v149
	v_mul_f32_e32 v153, v154, v154
	v_mul_f32_e32 v156, v155, v155
	v_pk_fma_f32 v[114:115], v[150:151], v[150:151], v[114:115] op_sel_hi:[1,1,0]
	v_pk_fma_f32 v[116:117], v[148:149], v[148:149], v[116:117] op_sel_hi:[1,1,0]
	s_min_i32 s6, s21, s18
	v_mov_b32_e32 v115, v153
	v_mov_b32_e32 v117, v156
	s_add_i32 s2, s6, 0xfffff800
	v_pk_add_f32 v[114:115], v[114:115], v[116:117]
	s_lshr_b32 s2, s2, 11
	v_pk_add_f32 v[112:113], v[112:113], v[114:115]
	s_cmpk_gt_i32 s6, 0x7ff
	v_add_f32_e32 v112, v112, v113
	s_cselect_b32 s7, s2, 8
	s_cmp_lg_u32 s7, s15
	v_add_f32_dpp v112, v112, v112 quad_perm:[1,0,3,2] row_mask:0xf bank_mask:0xf bound_ctrl:1
	s_cselect_b64 s[2:3], -1, 0
	s_add_u32 s4, s17, s7
	v_add_f32_dpp v112, v112, v112 quad_perm:[2,3,0,1] row_mask:0xf bank_mask:0xf bound_ctrl:1
	s_addc_u32 s5, s16, 0
	v_mov_b32_e32 v113, v173
	v_add_f32_dpp v112, v112, v112 row_half_mirror row_mask:0xf bank_mask:0xf bound_ctrl:1
	s_mulk_i32 s5, 0x6000
	s_mul_hi_u32 s8, s4, 0x6000
	v_add_f32_dpp v112, v112, v112 row_mirror row_mask:0xf bank_mask:0xf bound_ctrl:1
	s_add_i32 s8, s8, s5
	s_mulk_i32 s4, 0x6000
	v_mov_b32_dpp v113, v112 row_bcast:15 row_mask:0xa bank_mask:0xf
	v_add_f32_e32 v112, v112, v113
	v_mov_b32_e32 v113, v173
	s_add_u32 s4, s84, s4
	s_addc_u32 s5, s86, s8
	v_mov_b32_dpp v113, v112 row_bcast:31 row_mask:0xc bank_mask:0xf
	v_add_f32_e32 v112, v112, v113
	s_add_u32 s8, s4, 0x4000
	v_readlane_b32 s22, v112, 63
	s_addc_u32 s9, s5, 0
	v_mov_b64_e32 v[114:115], v[18:19]
	s_cmp_eq_u32 s7, s15
	v_mov_b64_e32 v[112:113], v[16:17]
	s_cbranch_scc1 .LBB0_1418
	v_lshl_add_u64 v[112:113], v[122:123], 2, s[8:9]
	global_load_dwordx4 v[112:115], v[112:113], off
	s_waitcnt vmcnt(0)
.LBB0_1418:
	v_lshl_add_u64 v[116:117], v[122:123], 2, s[4:5]
	s_mov_b64 s[4:5], 0x3000
	v_lshl_add_u64 v[152:153], v[116:117], 0, s[4:5]
	v_cndmask_b32_e64 v116, 0, 1, s[2:3]
	v_cmp_ne_u32_e64 s[4:5], 1, v116
	v_mov_b64_e32 v[118:119], v[22:23]
	s_andn2_b64 vcc, exec, s[2:3]
	v_mov_b64_e32 v[116:117], v[20:21]
	s_cbranch_vccnz .LBB0_1420
	global_load_dwordx4 v[116:119], v[152:153], off
	s_waitcnt vmcnt(0)
.LBB0_1420:
	v_fma_f32 v156, s22, v212, v198
	v_cmp_gt_f32_e32 vcc, s0, v156
	v_mul_f32_e32 v158, 0x4b800000, v156
	v_pk_add_f32 v[114:115], v[114:115], 1.0 op_sel_hi:[1,0]
	v_cndmask_b32_e32 v156, v156, v158, vcc
	v_rsq_f32_e32 v156, v156
	v_pk_add_f32 v[170:171], v[112:113], 1.0 op_sel_hi:[1,0]
	s_cmp_lt_i32 s21, s1
	s_cselect_b64 s[10:11], -1, 0
	v_mul_f32_e32 v158, 0x45800000, v156
	v_cndmask_b32_e32 v164, v156, v158, vcc
	v_pk_mul_f32 v[168:169], v[164:165], v[168:169] op_sel_hi:[0,1]
	v_pk_mul_f32 v[166:167], v[164:165], v[166:167] op_sel_hi:[0,1]
	v_pk_mul_f32 v[166:167], v[0:1], v[166:167]
	v_pk_mul_f32 v[168:169], v[2:3], v[168:169]
	s_ashr_i32 s7, s6, 31
	v_pk_fma_f32 v[112:113], v[168:169], v[114:115], v[118:119]
	v_pk_fma_f32 v[114:115], v[166:167], v[170:171], v[116:117]
	v_mov_b32_e32 v116, v173
	v_cvt_pk_fp8_f32 v116, v114, v115
	s_lshl_b64 s[2:3], s[6:7], 10
	v_readlane_b32 s6, v253, 44
	v_readlane_b32 s7, v253, 45
	v_cvt_pk_fp8_f32 v116, v112, v113 op_sel:[0,0,1]
	s_add_u32 s6, s6, s2
	s_addc_u32 s7, s7, s3
	s_cmp_ge_i32 s21, s1
	v_lshl_add_u64 v[166:167], s[6:7], 0, v[122:123]
	s_cbranch_scc1 .LBB0_1422
	global_store_dword v[166:167], v116, off
.LBB0_1422:
	v_cvt_f32_fp8_e32 v118, v116
	v_cvt_f32_fp8_sdwa v119, v116 src0_sel:BYTE_1
	v_cvt_f32_fp8_sdwa v156, v116 src0_sel:BYTE_2
	v_cvt_f32_fp8_sdwa v158, v116 src0_sel:BYTE_3
	v_sub_f32_e32 v114, v114, v118
	v_sub_f32_e32 v115, v115, v119
	v_cvt_pk_bf16_f32 v114, v114, v115
	v_sub_f32_e32 v112, v112, v156
	v_sub_f32_e32 v113, v113, v158
	v_cvt_pk_bf16_f32 v115, v112, v113
	v_cvt_pk_bf16_f32 v116, v118, v119
	v_cvt_pk_bf16_f32 v117, v156, v158
	ds_write_b64 v182, v[116:117]
	ds_write_b64 v183, v[114:115]
	v_mov_b64_e32 v[114:115], v[26:27]
	s_and_b64 vcc, exec, s[4:5]
	v_mov_b64_e32 v[112:113], v[24:25]
	s_cbranch_vccnz .LBB0_1424
	v_lshl_add_u64 v[112:113], v[126:127], 2, s[8:9]
	global_load_dwordx4 v[112:115], v[112:113], off
	s_waitcnt vmcnt(0)
.LBB0_1424:
	v_mov_b64_e32 v[118:119], v[34:35]
	s_and_b64 vcc, exec, s[4:5]
	v_mov_b64_e32 v[116:117], v[32:33]
	s_cbranch_vccnz .LBB0_1426
	global_load_dwordx4 v[116:119], v[152:153], off offset:1024
	s_waitcnt vmcnt(0)
.LBB0_1426:
	v_mov_b32_e32 v165, v164
	v_mov_b32_e32 v168, v161
	v_mov_b32_e32 v161, v162
	v_pk_mul_f32 v[160:161], v[164:165], v[160:161]
	v_pk_add_f32 v[112:113], v[112:113], 1.0 op_sel_hi:[1,0]
	v_pk_mul_f32 v[160:161], v[4:5], v[160:161]
	v_mov_b32_e32 v169, v163
	v_pk_fma_f32 v[112:113], v[160:161], v[112:113], v[116:117]
	v_mov_b32_e32 v116, v173
	v_mov_b32_e32 v170, v164
	v_mov_b32_e32 v171, v164
	v_cvt_pk_fp8_f32 v116, v112, v113
	v_pk_mul_f32 v[168:169], v[170:171], v[168:169]
	v_pk_add_f32 v[114:115], v[114:115], 1.0 op_sel_hi:[1,0]
	v_pk_mul_f32 v[160:161], v[6:7], v[168:169]
	v_cndmask_b32_e64 v117, 0, 1, s[10:11]
	v_pk_fma_f32 v[114:115], v[160:161], v[114:115], v[118:119]
	v_cmp_ne_u32_e64 s[6:7], 1, v117
	v_cvt_pk_fp8_f32 v116, v114, v115 op_sel:[0,0,1]
	s_andn2_b64 vcc, exec, s[10:11]
	s_cbranch_vccnz .LBB0_1428
	global_store_dword v[166:167], v116, off offset:256
.LBB0_1428:
	v_cvt_f32_fp8_e32 v118, v116
	v_cvt_f32_fp8_sdwa v119, v116 src0_sel:BYTE_1
	v_cvt_f32_fp8_sdwa v156, v116 src0_sel:BYTE_2
	v_cvt_f32_fp8_sdwa v158, v116 src0_sel:BYTE_3
	v_sub_f32_e32 v112, v112, v118
	v_sub_f32_e32 v113, v113, v119
	v_cvt_pk_bf16_f32 v112, v112, v113
	v_sub_f32_e32 v113, v114, v156
	v_sub_f32_e32 v114, v115, v158
	v_cvt_pk_bf16_f32 v113, v113, v114
	v_cvt_pk_bf16_f32 v116, v118, v119
	v_cvt_pk_bf16_f32 v117, v156, v158
	ds_write_b64 v182, v[116:117] offset:512
	ds_write_b64 v183, v[112:113] offset:512
	v_mov_b64_e32 v[114:115], v[30:31]
	s_and_b64 vcc, exec, s[4:5]
	v_mov_b64_e32 v[112:113], v[28:29]
	s_cbranch_vccnz .LBB0_1430
	v_lshl_add_u64 v[112:113], v[136:137], 2, s[8:9]
	global_load_dwordx4 v[112:115], v[112:113], off
	s_waitcnt vmcnt(0)
.LBB0_1430:
	v_mov_b64_e32 v[118:119], v[42:43]
	s_and_b64 vcc, exec, s[4:5]
	v_mov_b64_e32 v[116:117], v[40:41]
	s_cbranch_vccnz .LBB0_1432
	global_load_dwordx4 v[116:119], v[152:153], off offset:2048
	s_waitcnt vmcnt(0)
.LBB0_1432:
	v_pk_mul_f32 v[150:151], v[164:165], v[150:151]
	v_pk_add_f32 v[112:113], v[112:113], 1.0 op_sel_hi:[1,0]
	v_pk_mul_f32 v[150:151], v[8:9], v[150:151]
	v_mov_b32_e32 v160, v164
	v_pk_fma_f32 v[112:113], v[150:151], v[112:113], v[116:117]
	v_mov_b32_e32 v116, v173
	v_mov_b32_e32 v161, v164
	v_cvt_pk_fp8_f32 v116, v112, v113
	v_pk_mul_f32 v[148:149], v[160:161], v[148:149]
	v_pk_add_f32 v[114:115], v[114:115], 1.0 op_sel_hi:[1,0]
	v_pk_mul_f32 v[148:149], v[10:11], v[148:149]
	s_and_b64 vcc, exec, s[6:7]
	v_pk_fma_f32 v[114:115], v[148:149], v[114:115], v[118:119]
	s_nop 0
	v_cvt_pk_fp8_f32 v116, v114, v115 op_sel:[0,0,1]
	s_cbranch_vccnz .LBB0_1434
	global_store_dword v[166:167], v116, off offset:512
.LBB0_1434:
	v_cvt_f32_fp8_e32 v118, v116
	v_cvt_f32_fp8_sdwa v119, v116 src0_sel:BYTE_1
	v_cvt_f32_fp8_sdwa v148, v116 src0_sel:BYTE_2
	v_cvt_f32_fp8_sdwa v149, v116 src0_sel:BYTE_3
	v_sub_f32_e32 v112, v112, v118
	v_sub_f32_e32 v113, v113, v119
	v_cvt_pk_bf16_f32 v112, v112, v113
	v_sub_f32_e32 v113, v114, v148
	v_sub_f32_e32 v114, v115, v149
	v_cvt_pk_bf16_f32 v113, v113, v114
	v_cvt_pk_bf16_f32 v116, v118, v119
	v_cvt_pk_bf16_f32 v117, v148, v149
	ds_write_b64 v182, v[116:117] offset:1024
	ds_write_b64 v183, v[112:113] offset:1024
	v_mov_b64_e32 v[114:115], v[38:39]
	s_and_b64 vcc, exec, s[4:5]
	v_mov_b64_e32 v[112:113], v[36:37]
	s_cbranch_vccnz .LBB0_1436
	v_lshl_add_u64 v[112:113], v[138:139], 2, s[8:9]
	global_load_dwordx4 v[112:115], v[112:113], off
	s_waitcnt vmcnt(0)
.LBB0_1436:
	v_mov_b64_e32 v[118:119], v[46:47]
	s_and_b64 vcc, exec, s[4:5]
	v_mov_b64_e32 v[116:117], v[44:45]
	s_cbranch_vccnz .LBB0_1438
	global_load_dwordx4 v[116:119], v[152:153], off offset:3072
	s_waitcnt vmcnt(0)
.LBB0_1438:
	v_mov_b32_e32 v156, v159
	v_pk_mul_f32 v[150:151], v[156:157], v[164:165]
	v_pk_add_f32 v[112:113], v[112:113], 1.0 op_sel_hi:[1,0]
	v_pk_mul_f32 v[150:151], v[12:13], v[150:151]
	v_mov_b32_e32 v148, v164
	v_pk_fma_f32 v[112:113], v[150:151], v[112:113], v[116:117]
	v_mov_b32_e32 v116, v173
	v_mov_b32_e32 v149, v164
	v_cvt_pk_fp8_f32 v116, v112, v113
	v_pk_mul_f32 v[148:149], v[154:155], v[148:149]
	v_pk_add_f32 v[114:115], v[114:115], 1.0 op_sel_hi:[1,0]
	v_pk_mul_f32 v[148:149], v[14:15], v[148:149]
	s_and_b64 vcc, exec, s[6:7]
	v_pk_fma_f32 v[114:115], v[148:149], v[114:115], v[118:119]
	s_nop 0
	v_cvt_pk_fp8_f32 v116, v114, v115 op_sel:[0,0,1]
	s_cbranch_vccnz .LBB0_1391
	global_store_dword v[166:167], v116, off offset:768
	s_branch .LBB0_1391
